# speedup vs baseline: 1.0082x; 1.0082x over previous
.LBB1_8:
	s_or_b64 exec, exec, s[4:5]
	s_waitcnt vmcnt(1)
	v_mov_b32_e32 v184, 1
	v_lshl_add_u32 v180, v176, 2, v172
	v_lshl_add_u32 v181, v177, 2, v172
	v_lshl_add_u32 v182, v178, 2, v172
	v_lshl_add_u32 v183, v179, 2, v172
	s_waitcnt lgkmcnt(0)
	ds_add_u32 v180, v184
	ds_add_u32 v181, v184
	ds_add_u32 v182, v184
	ds_add_u32 v183, v184
	s_waitcnt lgkmcnt(0)
	ds_read_b32 v151, v173
	s_waitcnt lgkmcnt(0)
	v_cvt_f32_i32_e32 v185, v151
	ds_write_b32 v173, v185 offset:256
	v_add_u32_e32 v10, v172, v2
	s_waitcnt vmcnt(1) lgkmcnt(0)
	s_barrier
	s_nop 0
	s_nop 0
	s_nop 0
	s_nop 0
	s_nop 0
	ds_read_b128 v[18:21], v10 offset:256
	ds_read_b128 v[22:25], v10 offset:288
	ds_read_b128 v[82:85], v10 offset:320
	ds_read_b128 v[86:89], v10 offset:352
	ds_read_b128 v[74:77], v10 offset:384
	ds_read_b128 v[78:81], v10 offset:416
	ds_read_b128 v[2:5], v213 offset:32768
	ds_read_b128 v[6:9], v213 offset:0
	ds_read_b128 v[66:69], v10 offset:448
	ds_read_b128 v[70:73], v10 offset:480
	ds_read_b128 v[10:13], v213 offset:1024
	s_waitcnt lgkmcnt(3)
	v_pk_mul_f32 v[26:27], v[8:9], v[20:21]
	v_pk_mul_f32 v[28:29], v[6:7], v[18:19]
	ds_read_b128 v[14:17], v213 offset:8192
	s_waitcnt lgkmcnt(1)
	v_pk_mul_f32 v[12:13], v[12:13], v[24:25]
	v_pk_mul_f32 v[10:11], v[10:11], v[22:23]
	v_pk_fma_f32 v[30:31], v[8:9], v[20:21], v[12:13]
	v_pk_fma_f32 v[32:33], v[6:7], v[18:19], v[10:11]
	v_cvt_pk_bf16_f32 v9, v12, v13
	v_cvt_pk_bf16_f32 v7, v26, v27
	v_cvt_pk_bf16_f32 v8, v10, v11
	v_cvt_pk_bf16_f32 v6, v28, v29
	ds_read_b128 v[10:13], v213 offset:33792
	s_nop 0
	v_mfma_f32_32x32x16_bf16 v[34:49], v[2:5], v[6:9], 0
	ds_read_b128 v[6:9], v213 offset:9216
	s_waitcnt lgkmcnt(2)
	v_mul_f32_e32 v26, v16, v20
	v_mul_f32_e32 v27, v17, v21
	v_pk_mul_f32 v[50:51], v[14:15], v[18:19]
	s_mov_b32 s4, 0x3727c5ac
	s_waitcnt lgkmcnt(0)
	v_pk_mul_f32 v[8:9], v[8:9], v[24:25]
	v_pk_mul_f32 v[28:29], v[6:7], v[22:23]
	v_pk_fma_f32 v[90:91], v[16:17], v[20:21], v[8:9]
	v_pk_fma_f32 v[92:93], v[14:15], v[18:19], v[28:29]
	ds_read_b128 v[14:17], v213 offset:2048
	v_cvt_pk_bf16_f32 v9, v8, v9
	v_cvt_pk_bf16_f32 v7, v26, v27
	v_cvt_pk_bf16_f32 v8, v28, v29
	ds_read_b128 v[26:29], v213 offset:3072
	v_cvt_pk_bf16_f32 v6, v50, v51
	s_waitcnt lgkmcnt(1)
	v_pk_mul_f32 v[94:95], v[14:15], v[82:83]
	s_mov_b32 s0, 0x3c800000
	v_mfma_f32_32x32x16_bf16 v[50:65], v[2:5], v[6:9], 0
	v_mul_f32_e32 v2, v16, v84
	v_mul_f32_e32 v3, v17, v85
	s_waitcnt lgkmcnt(0)
	v_mul_f32_e32 v4, v28, v88
	v_mul_f32_e32 v5, v29, v89
	v_pk_mul_f32 v[6:7], v[26:27], v[86:87]
	v_pk_fma_f32 v[8:9], v[16:17], v[84:85], v[4:5]
	v_cvt_pk_bf16_f32 v3, v2, v3
	v_pk_fma_f32 v[14:15], v[14:15], v[82:83], v[6:7]
	v_pk_add_f32 v[26:27], v[8:9], v[30:31]
	v_cvt_pk_bf16_f32 v5, v4, v5
	v_cvt_pk_bf16_f32 v4, v6, v7
	ds_read_b128 v[6:9], v213 offset:10240
	v_pk_add_f32 v[28:29], v[14:15], v[32:33]
	ds_read_b128 v[14:17], v213 offset:11264
	v_cvt_pk_bf16_f32 v2, v94, v95
	s_waitcnt lgkmcnt(1)
	v_pk_mul_f32 v[30:31], v[6:7], v[82:83]
	v_mov_b64_e32 v[152:153], s[4:5]
	v_mfma_f32_32x32x16_bf16 v[34:49], v[10:13], v[2:5], v[34:49]
	v_mul_f32_e32 v2, v8, v84
	v_mul_f32_e32 v3, v9, v85
	s_waitcnt lgkmcnt(0)
	v_mul_f32_e32 v4, v16, v88
	v_mul_f32_e32 v5, v17, v89
	v_pk_mul_f32 v[14:15], v[14:15], v[86:87]
	v_pk_fma_f32 v[8:9], v[8:9], v[84:85], v[4:5]
	v_pk_fma_f32 v[6:7], v[6:7], v[82:83], v[14:15]
	v_cvt_pk_bf16_f32 v5, v4, v5
	v_cvt_pk_bf16_f32 v3, v2, v3
	v_cvt_pk_bf16_f32 v4, v14, v15
	v_pk_add_f32 v[32:33], v[8:9], v[90:91]
	v_pk_add_f32 v[90:91], v[6:7], v[92:93]
	ds_read_b128 v[6:9], v213 offset:34816
	ds_read_b128 v[14:17], v213 offset:4096
	v_cvt_pk_bf16_f32 v2, v30, v31
	s_mov_b32 s13, 0
	s_mov_b64 s[6:7], 0
	v_mfma_f32_32x32x16_bf16 v[50:65], v[10:13], v[2:5], v[50:65]
	ds_read_b128 v[2:5], v213 offset:5120
	ds_read_b128 v[10:13], v213 offset:12288
	s_waitcnt lgkmcnt(2)
	v_pk_mul_f32 v[30:31], v[16:17], v[76:77]
	v_pk_mul_f32 v[92:93], v[14:15], v[74:75]
	s_waitcnt lgkmcnt(1)
	v_pk_mul_f32 v[4:5], v[4:5], v[80:81]
	v_pk_mul_f32 v[94:95], v[2:3], v[78:79]
	v_pk_fma_f32 v[2:3], v[16:17], v[76:77], v[4:5]
	v_cvt_pk_bf16_f32 v5, v4, v5
	v_pk_add_f32 v[96:97], v[2:3], v[26:27]
	v_cvt_pk_bf16_f32 v3, v30, v31
	v_cvt_pk_bf16_f32 v4, v94, v95
	v_cvt_pk_bf16_f32 v2, v92, v93
	v_pk_fma_f32 v[14:15], v[14:15], v[74:75], v[94:95]
	s_waitcnt lgkmcnt(0)
	v_pk_mul_f32 v[30:31], v[10:11], v[74:75]
	v_mfma_f32_32x32x16_bf16 v[34:49], v[6:9], v[2:5], v[34:49]
	ds_read_b128 v[2:5], v213 offset:13312
	v_add_f32_e32 v98, v14, v28
	v_add_f32_e32 v99, v15, v29
	ds_read_b128 v[14:17], v213 offset:35840
	v_pk_mul_f32 v[26:27], v[12:13], v[76:77]
	s_waitcnt lgkmcnt(1)
	v_pk_mul_f32 v[4:5], v[4:5], v[80:81]
	v_pk_mul_f32 v[28:29], v[2:3], v[78:79]
	v_pk_fma_f32 v[2:3], v[12:13], v[76:77], v[4:5]
	v_pk_fma_f32 v[10:11], v[10:11], v[74:75], v[28:29]
	v_pk_add_f32 v[32:33], v[2:3], v[32:33]
	v_pk_add_f32 v[92:93], v[10:11], v[90:91]
	ds_read_b128 v[10:13], v213 offset:6144
	v_cvt_pk_bf16_f32 v5, v4, v5
	v_cvt_pk_bf16_f32 v3, v26, v27
	v_cvt_pk_bf16_f32 v4, v28, v29
	ds_read_b128 v[26:29], v213 offset:7168
	v_cvt_pk_bf16_f32 v2, v30, v31
	s_waitcnt lgkmcnt(1)
	v_pk_mul_f32 v[30:31], v[10:11], v[66:67]
	v_mfma_f32_32x32x16_bf16 v[50:65], v[6:9], v[2:5], v[50:65]
	v_mul_f32_e32 v2, v12, v68
	v_mul_f32_e32 v3, v13, v69
	s_waitcnt lgkmcnt(0)
	v_mul_f32_e32 v4, v28, v72
	v_mul_f32_e32 v5, v29, v73
	v_pk_mul_f32 v[6:7], v[26:27], v[70:71]
	v_pk_fma_f32 v[8:9], v[12:13], v[68:69], v[4:5]
	v_cvt_pk_bf16_f32 v3, v2, v3
	v_pk_fma_f32 v[10:11], v[10:11], v[66:67], v[6:7]
	v_pk_add_f32 v[94:95], v[8:9], v[96:97]
	v_cvt_pk_bf16_f32 v5, v4, v5
	v_cvt_pk_bf16_f32 v4, v6, v7
	ds_read_b128 v[6:9], v213 offset:14336
	v_pk_add_f32 v[96:97], v[10:11], v[98:99]
	ds_read_b128 v[10:13], v213 offset:15360
	v_cvt_pk_bf16_f32 v2, v30, v31
	s_waitcnt lgkmcnt(1)
	v_pk_mul_f32 v[30:31], v[6:7], v[66:67]
	v_mfma_f32_32x32x16_bf16 v[34:49], v[14:17], v[2:5], v[34:49]
	s_waitcnt lgkmcnt(0)
	v_mul_f32_e32 v10, v10, v70
	v_mul_f32_e32 v11, v11, v71
	v_mul_f32_e32 v2, v8, v68
	v_mul_f32_e32 v3, v9, v69
	v_pk_mul_f32 v[4:5], v[12:13], v[72:73]
	v_pk_fma_f32 v[6:7], v[6:7], v[66:67], v[10:11]
	v_pk_fma_f32 v[8:9], v[8:9], v[68:69], v[4:5]
	v_pk_add_f32 v[92:93], v[6:7], v[92:93]
	v_cvt_pk_bf16_f32 v3, v2, v3
	v_pk_add_f32 v[90:91], v[8:9], v[32:33]
	v_cvt_pk_bf16_f32 v5, v4, v5
	v_cvt_pk_bf16_f32 v4, v10, v11
	ds_read_b128 v[26:29], v213 offset:36864
	ds_read_b128 v[6:9], v213 offset:16384
	v_cvt_pk_bf16_f32 v2, v30, v31
	ds_read_b128 v[98:101], v213 offset:25600
	ds_read_b128 v[102:105], v213 offset:37888
	v_mfma_f32_32x32x16_bf16 v[50:65], v[14:17], v[2:5], v[50:65]
	ds_read_b128 v[2:5], v213 offset:17408
	ds_read_b128 v[30:33], v213 offset:24576
	s_waitcnt lgkmcnt(4)
	v_pk_mul_f32 v[12:13], v[6:7], v[18:19]
	v_pk_mul_f32 v[10:11], v[8:9], v[20:21]
	s_waitcnt lgkmcnt(1)
	v_pk_mul_f32 v[14:15], v[2:3], v[22:23]
	v_pk_mul_f32 v[22:23], v[98:99], v[22:23]
	v_pk_fma_f32 v[112:113], v[6:7], v[18:19], v[14:15]
	s_waitcnt lgkmcnt(0)
	v_pk_mul_f32 v[114:115], v[30:31], v[18:19]
	v_pk_fma_f32 v[118:119], v[30:31], v[18:19], v[22:23]
	v_pk_mul_f32 v[4:5], v[4:5], v[24:25]
	v_pk_mul_f32 v[106:107], v[32:33], v[20:21]
	v_pk_mul_f32 v[24:25], v[100:101], v[24:25]
	ds_read_b128 v[98:101], v213 offset:18432
	v_cvt_pk_bf16_f32 v19, v106, v107
	ds_read_b128 v[106:109], v213 offset:19456
	v_pk_fma_f32 v[110:111], v[8:9], v[20:21], v[4:5]
	v_cvt_pk_bf16_f32 v5, v4, v5
	v_cvt_pk_bf16_f32 v3, v10, v11
	v_cvt_pk_bf16_f32 v4, v14, v15
	s_waitcnt lgkmcnt(0)
	v_pk_mul_f32 v[106:107], v[106:107], v[86:87]
	v_cvt_pk_bf16_f32 v2, v12, v13
	v_pk_mul_f32 v[120:121], v[98:99], v[82:83]
	v_pk_mul_f32 v[108:109], v[108:109], v[88:89]
	v_pk_fma_f32 v[98:99], v[98:99], v[82:83], v[106:107]
	v_mfma_f32_32x32x16_bf16 v[2:17], v[26:29], v[2:5], 0
	v_cvt_pk_bf16_f32 v18, v114, v115
	v_mul_f32_e32 v114, v100, v84
	v_mul_f32_e32 v115, v101, v85
	v_fma_f32 v100, v100, v84, v108
	v_fma_f32 v101, v101, v85, v109
	v_pk_add_f32 v[124:125], v[98:99], v[112:113]
	v_pk_add_f32 v[122:123], v[100:101], v[110:111]
	v_cvt_pk_bf16_f32 v101, v108, v109
	v_cvt_pk_bf16_f32 v100, v106, v107
	ds_read_b128 v[106:109], v213 offset:26624
	v_pk_fma_f32 v[116:117], v[32:33], v[20:21], v[24:25]
	v_cvt_pk_bf16_f32 v21, v24, v25
	v_cvt_pk_bf16_f32 v20, v22, v23
	ds_read_b128 v[110:113], v213 offset:27648
	v_cvt_pk_bf16_f32 v99, v114, v115
	v_mfma_f32_32x32x16_bf16 v[18:33], v[26:29], v[18:21], 0
	v_cvt_pk_bf16_f32 v98, v120, v121
	s_waitcnt lgkmcnt(1)
	v_mul_f32_e32 v114, v106, v82
	v_mul_f32_e32 v115, v107, v83
	s_waitcnt lgkmcnt(0)
	v_pk_mul_f32 v[86:87], v[110:111], v[86:87]
	v_pk_mul_f32 v[88:89], v[112:113], v[88:89]
	v_pk_fma_f32 v[82:83], v[106:107], v[82:83], v[86:87]
	v_mfma_f32_32x32x16_bf16 v[2:17], v[102:105], v[98:101], v[2:17]
	v_mul_f32_e32 v98, v108, v84
	v_mul_f32_e32 v99, v109, v85
	v_fma_f32 v84, v108, v84, v88
	v_fma_f32 v85, v109, v85, v89
	v_add_f32_e32 v108, v82, v118
	v_add_f32_e32 v109, v83, v119
	v_cvt_pk_bf16_f32 v83, v98, v99
	v_pk_add_f32 v[106:107], v[84:85], v[116:117]
	v_cvt_pk_bf16_f32 v85, v88, v89
	v_cvt_pk_bf16_f32 v84, v86, v87
	ds_read_b128 v[86:89], v213 offset:38912
	ds_read_b128 v[98:101], v213 offset:20480
	v_cvt_pk_bf16_f32 v82, v114, v115
	s_waitcnt lgkmcnt(0)
	v_pk_mul_f32 v[110:111], v[100:101], v[76:77]
	v_mfma_f32_32x32x16_bf16 v[18:33], v[102:105], v[82:85], v[18:33]
	ds_read_b128 v[82:85], v213 offset:21504
	ds_read_b128 v[102:105], v213 offset:28672
	v_mul_f32_e32 v112, v98, v74
	v_mul_f32_e32 v113, v99, v75
	s_waitcnt lgkmcnt(1)
	v_pk_mul_f32 v[84:85], v[84:85], v[80:81]
	v_pk_mul_f32 v[114:115], v[82:83], v[78:79]
	v_pk_fma_f32 v[82:83], v[100:101], v[76:77], v[84:85]
	v_cvt_pk_bf16_f32 v85, v84, v85
	v_pk_add_f32 v[116:117], v[82:83], v[122:123]
	v_cvt_pk_bf16_f32 v83, v110, v111
	v_cvt_pk_bf16_f32 v84, v114, v115
	v_cvt_pk_bf16_f32 v82, v112, v113
	v_pk_fma_f32 v[98:99], v[98:99], v[74:75], v[114:115]
	s_waitcnt lgkmcnt(0)
	v_pk_mul_f32 v[112:113], v[102:103], v[74:75]
	v_mfma_f32_32x32x16_bf16 v[2:17], v[86:89], v[82:85], v[2:17]
	ds_read_b128 v[82:85], v213 offset:29696
	v_add_f32_e32 v118, v98, v124
	v_add_f32_e32 v119, v99, v125
	v_mul_f32_e32 v110, v104, v76
	v_mul_f32_e32 v111, v105, v77
	ds_read_b128 v[98:101], v213 offset:39936
	s_waitcnt lgkmcnt(1)
	v_pk_mul_f32 v[78:79], v[82:83], v[78:79]
	v_pk_mul_f32 v[80:81], v[84:85], v[80:81]
	v_pk_fma_f32 v[74:75], v[102:103], v[74:75], v[78:79]
	v_pk_fma_f32 v[76:77], v[104:105], v[76:77], v[80:81]
	v_pk_add_f32 v[104:105], v[74:75], v[108:109]
	v_pk_add_f32 v[102:103], v[76:77], v[106:107]
	v_cvt_pk_bf16_f32 v77, v80, v81
	v_cvt_pk_bf16_f32 v76, v78, v79
	ds_read_b128 v[78:81], v213 offset:22528
	ds_read_b128 v[82:85], v213 offset:23552
	v_cvt_pk_bf16_f32 v75, v110, v111
	v_cvt_pk_bf16_f32 v74, v112, v113
	s_waitcnt lgkmcnt(0)
	v_pk_mul_f32 v[82:83], v[82:83], v[70:71]
	v_mfma_f32_32x32x16_bf16 v[18:33], v[86:89], v[74:77], v[18:33]
	v_mul_f32_e32 v74, v80, v68
	v_mul_f32_e32 v75, v81, v69
	v_mul_f32_e32 v76, v84, v72
	v_mul_f32_e32 v77, v85, v73
	v_mul_f32_e32 v86, v78, v66
	v_mul_f32_e32 v87, v79, v67
	v_pk_fma_f32 v[80:81], v[80:81], v[68:69], v[76:77]
	v_pk_fma_f32 v[78:79], v[78:79], v[66:67], v[82:83]
	v_cvt_pk_bf16_f32 v75, v74, v75
	v_pk_add_f32 v[88:89], v[80:81], v[116:117]
	v_pk_add_f32 v[106:107], v[78:79], v[118:119]
	ds_read_b128 v[78:81], v213 offset:30720
	v_cvt_pk_bf16_f32 v77, v76, v77
	v_cvt_pk_bf16_f32 v76, v82, v83
	ds_read_b128 v[82:85], v213 offset:31744
	v_cvt_pk_bf16_f32 v74, v86, v87
	s_waitcnt lgkmcnt(0)
	v_pk_mul_f32 v[72:73], v[84:85], v[72:73]
	v_mfma_f32_32x32x16_bf16 v[2:17], v[98:101], v[74:77], v[2:17]
	v_mul_f32_e32 v74, v80, v68
	v_mul_f32_e32 v75, v81, v69
	v_fma_f32 v68, v80, v68, v72
	v_fma_f32 v69, v81, v69, v73
	v_mul_f32_e32 v70, v82, v70
	v_mul_f32_e32 v71, v83, v71
	v_pk_add_f32 v[84:85], v[68:69], v[102:103]
	v_cvt_pk_bf16_f32 v69, v72, v73
	v_add_f32_e32 v72, v97, v96
	v_add_f32_e32 v73, v94, v95
	v_pk_mul_f32 v[76:77], v[78:79], v[66:67]
	v_pk_fma_f32 v[66:67], v[78:79], v[66:67], v[70:71]
	v_add_f32_e32 v72, v72, v73
	v_pk_add_f32 v[86:87], v[66:67], v[104:105]
	v_mov_b32_e32 v66, v72
	s_nop 1
	v_permlane32_swap_b32_e32 v72, v66
	v_add_f32_e32 v66, v72, v66
	v_cvt_pk_bf16_f32 v67, v74, v75
	v_rcp_f32_e32 v74, v66
	v_cvt_pk_bf16_f32 v68, v70, v71
	v_cvt_pk_bf16_f32 v66, v76, v77
	v_pk_mul_f32 v[70:71], v[46:47], v[74:75] op_sel_hi:[1,0]
	s_nop 0
	v_mfma_f32_32x32x16_bf16 v[18:33], v[98:101], v[66:69], v[18:33]
	v_mul_f32_e32 v66, v42, v74
	v_mul_f32_e32 v67, v43, v74
	v_add_f32_e32 v42, v93, v92
	v_add_f32_e32 v43, v90, v91
	v_pk_mul_f32 v[68:69], v[44:45], v[74:75] op_sel_hi:[1,0]
	v_add_f32_e32 v42, v42, v43
	v_mov_b32_e32 v43, v42
	s_nop 1
	v_permlane32_swap_b32_e32 v42, v43
	v_add_f32_e32 v42, v42, v43
	v_rcp_f32_e32 v42, v42
	v_add_f32_e32 v44, v107, v106
	v_add_f32_e32 v45, v88, v89
	v_pk_mul_f32 v[72:73], v[48:49], v[74:75] op_sel_hi:[1,0]
	v_add_f32_e32 v44, v44, v45
	v_pk_mul_f32 v[36:37], v[36:37], v[74:75] op_sel_hi:[1,0]
	v_pk_mul_f32 v[38:39], v[38:39], v[74:75] op_sel_hi:[1,0]
	v_pk_mul_f32 v[40:41], v[40:41], v[74:75] op_sel_hi:[1,0]
	v_pk_mul_f32 v[34:35], v[34:35], v[74:75] op_sel_hi:[1,0]
	v_pk_mul_f32 v[74:75], v[58:59], v[42:43] op_sel_hi:[1,0]
	v_pk_mul_f32 v[78:79], v[60:61], v[42:43] op_sel_hi:[1,0]
	v_pk_mul_f32 v[80:81], v[62:63], v[42:43] op_sel_hi:[1,0]
	v_pk_mul_f32 v[82:83], v[64:65], v[42:43] op_sel_hi:[1,0]
	v_pk_mul_f32 v[92:93], v[52:53], v[42:43] op_sel_hi:[1,0]
	v_mov_b32_e32 v43, v44
	s_nop 1
	v_permlane32_swap_b32_e32 v44, v43
	v_add_f32_e32 v43, v44, v43
	v_rcp_f32_e32 v76, v43
	v_pk_mul_f32 v[96:97], v[54:55], v[42:43] op_sel_hi:[1,0]
	v_pk_mul_f32 v[94:95], v[56:57], v[42:43] op_sel_hi:[1,0]
	v_pk_mul_f32 v[98:99], v[50:51], v[42:43] op_sel_hi:[1,0]
	v_pk_mul_f32 v[100:101], v[4:5], v[76:77] op_sel_hi:[1,0]
	v_pk_mov_b32 v[4:5], v[86:87], v[84:85] op_sel:[1,0]
	v_mov_b32_e32 v87, v85
	v_pk_add_f32 v[4:5], v[4:5], v[86:87]
	v_pk_mul_f32 v[102:103], v[6:7], v[76:77] op_sel_hi:[1,0]
	v_pk_add_f32 v[104:105], v[4:5], v[4:5] op_sel:[0,1] op_sel_hi:[1,0]
	v_cvt_pk_bf16_f32 v7, v40, v41
	ds_read_b128 v[84:87], v150 offset:52224
	ds_read_b128 v[50:53], v150 offset:35840
	ds_read_b128 v[54:57], v150 offset:36864
	ds_read_b128 v[58:61], v150 offset:37888
	ds_read_b128 v[62:65], v150 offset:38912
	v_cvt_pk_bf16_f32 v6, v38, v39
	v_cvt_pk_bf16_f32 v5, v36, v37
	v_cvt_pk_bf16_f32 v4, v34, v35
	ds_read_b128 v[88:91], v150 offset:53248
	ds_read_b128 v[34:37], v150 offset:39936
	ds_read_b128 v[38:41], v150 offset:40960
	ds_read_b128 v[42:45], v150 offset:41984
	ds_read_b128 v[46:49], v150 offset:43008
	v_cvt_pk_bf16_f32 v95, v94, v95
	v_cvt_pk_bf16_f32 v94, v96, v97
	v_cvt_pk_bf16_f32 v93, v92, v93
	v_cvt_pk_bf16_f32 v92, v98, v99
	s_waitcnt lgkmcnt(5)
	v_mfma_f32_32x32x16_bf16 v[50:65], v[84:87], v[4:7], v[50:65]
	v_mul_f32_e32 v10, v10, v76
	v_mul_f32_e32 v11, v11, v76
	v_mul_f32_e32 v12, v12, v76
	v_mul_f32_e32 v13, v13, v76
	v_mul_f32_e32 v8, v8, v76
	v_mul_f32_e32 v9, v9, v76
	v_mov_b32_e32 v77, v104
	s_nop 1
	v_permlane32_swap_b32_e32 v104, v77
	v_cvt_pk_bf16_f32 v73, v72, v73
	s_waitcnt lgkmcnt(0)
	v_mfma_f32_32x32x16_bf16 v[34:49], v[84:87], v[92:95], v[34:49]
	v_cvt_pk_bf16_f32 v72, v70, v71
	v_cvt_pk_bf16_f32 v70, v66, v67
	v_add_f32_e32 v66, v104, v77
	v_cvt_pk_bf16_f32 v71, v68, v69
	v_rcp_f32_e32 v104, v66
	v_cvt_pk_bf16_f32 v69, v82, v83
	v_cvt_pk_bf16_f32 v68, v80, v81
	v_cvt_pk_bf16_f32 v67, v78, v79
	v_cvt_pk_bf16_f32 v66, v74, v75
	ds_read_b128 v[78:81], v150 offset:54272
	v_mfma_f32_32x32x16_bf16 v[50:65], v[88:91], v[70:73], v[50:65]
	v_mul_f32_e32 v2, v2, v76
	v_mul_f32_e32 v3, v3, v76
	v_mul_f32_e32 v20, v20, v104
	v_mul_f32_e32 v21, v21, v104
	v_cvt_pk_bf16_f32 v85, v8, v9
	v_cvt_pk_bf16_f32 v82, v2, v3
	v_pk_mul_f32 v[2:3], v[22:23], v[104:105] op_sel_hi:[1,0]
	v_pk_mul_f32 v[8:9], v[24:25], v[104:105] op_sel_hi:[1,0]
	v_pk_mul_f32 v[18:19], v[18:19], v[104:105] op_sel_hi:[1,0]
	v_mfma_f32_32x32x16_bf16 v[34:49], v[88:91], v[66:69], v[34:49]
	v_cvt_pk_bf16_f32 v84, v102, v103
	v_cvt_pk_bf16_f32 v83, v100, v101
	ds_read_b128 v[86:89], v150 offset:55296
	v_cvt_pk_bf16_f32 v99, v8, v9
	v_cvt_pk_bf16_f32 v98, v2, v3
	v_cvt_pk_bf16_f32 v97, v20, v21
	v_cvt_pk_bf16_f32 v96, v18, v19
	s_waitcnt lgkmcnt(1)
	v_mfma_f32_32x32x16_bf16 v[50:65], v[78:81], v[82:85], v[50:65]
	v_mul_f32_e32 v2, v14, v76
	v_mul_f32_e32 v3, v15, v76
	v_mul_f32_e32 v8, v16, v76
	v_mul_f32_e32 v9, v17, v76
	v_mul_f32_e32 v14, v26, v104
	v_mul_f32_e32 v15, v27, v104
	v_cvt_pk_bf16_f32 v77, v8, v9
	v_cvt_pk_bf16_f32 v76, v2, v3
	v_cvt_pk_bf16_f32 v74, v10, v11
	v_pk_mul_f32 v[2:3], v[28:29], v[104:105] op_sel_hi:[1,0]
	v_mfma_f32_32x32x16_bf16 v[34:49], v[78:81], v[96:99], v[34:49]
	v_mul_f32_e32 v8, v30, v104
	v_mul_f32_e32 v9, v31, v104
	v_mul_f32_e32 v10, v32, v104
	v_mul_f32_e32 v11, v33, v104
	v_cvt_pk_bf16_f32 v75, v12, v13
	v_cvt_pk_bf16_f32 v81, v10, v11
	v_cvt_pk_bf16_f32 v80, v8, v9
	v_cvt_pk_bf16_f32 v79, v2, v3
	v_cvt_pk_bf16_f32 v78, v14, v15
	s_waitcnt lgkmcnt(0)
	v_mfma_f32_32x32x16_bf16 v[50:65], v[86:89], v[74:77], v[50:65]
	v_mfma_f32_32x32x16_bf16 v[34:49], v[86:89], v[78:81], v[34:49]
	ds_read_b128 v[86:89], v150 offset:56320
	ds_read_b128 v[18:21], v150 offset:44032
	ds_read_b128 v[22:25], v150 offset:45056
	ds_read_b128 v[26:29], v150 offset:46080
	ds_read_b128 v[30:33], v150 offset:47104
	ds_read_b128 v[100:103], v150 offset:57344
	s_waitcnt lgkmcnt(1)
	v_mfma_f32_32x32x16_bf16 v[18:33], v[86:89], v[4:7], v[18:33]
	ds_read_b128 v[2:5], v150 offset:48128
	ds_read_b128 v[6:9], v150 offset:49152
	ds_read_b128 v[10:13], v150 offset:50176
	ds_read_b128 v[14:17], v150 offset:51200
	s_waitcnt lgkmcnt(0)
	v_mfma_f32_32x32x16_bf16 v[2:17], v[86:89], v[92:95], v[2:17]
	v_mfma_f32_32x32x16_bf16 v[18:33], v[100:103], v[70:73], v[18:33]
	v_mfma_f32_32x32x16_bf16 v[2:17], v[100:103], v[66:69], v[2:17]
	ds_read_b128 v[66:69], v150 offset:58368
	ds_read_b128 v[70:73], v150 offset:59392
	s_waitcnt lgkmcnt(1)
	v_mfma_f32_32x32x16_bf16 v[18:33], v[66:69], v[82:85], v[18:33]
	v_mfma_f32_32x32x16_bf16 v[2:17], v[66:69], v[96:99], v[2:17]
	s_waitcnt lgkmcnt(0)
	v_mfma_f32_32x32x16_bf16 v[18:33], v[70:73], v[74:77], v[18:33]
	v_mfma_f32_32x32x16_bf16 v[2:17], v[70:73], v[78:81], v[2:17]
	s_nop 10
	v_mul_f32_e32 v66, v22, v22
	v_mul_f32_e32 v67, v23, v23
	v_mul_f32_e32 v68, v30, v30
	v_mul_f32_e32 v69, v31, v31
	v_mul_f32_e32 v70, v24, v24
	v_mul_f32_e32 v71, v25, v25
	v_pk_mul_f32 v[72:73], v[32:33], v[32:33]
	v_pk_mul_f32 v[74:75], v[20:21], v[20:21]
	v_pk_mul_f32 v[76:77], v[28:29], v[28:29]
	v_pk_mul_f32 v[78:79], v[26:27], v[26:27]
	v_pk_mul_f32 v[80:81], v[18:19], v[18:19]
	v_pk_fma_f32 v[78:79], v[58:59], v[58:59], v[78:79]
	v_pk_fma_f32 v[76:77], v[60:61], v[60:61], v[76:77]
	v_pk_fma_f32 v[74:75], v[52:53], v[52:53], v[74:75]
	v_pk_fma_f32 v[72:73], v[64:65], v[64:65], v[72:73]
	v_pk_fma_f32 v[70:71], v[56:57], v[56:57], v[70:71]
	v_pk_fma_f32 v[68:69], v[62:63], v[62:63], v[68:69]
	v_pk_fma_f32 v[66:67], v[54:55], v[54:55], v[66:67]
	v_pk_fma_f32 v[80:81], v[50:51], v[50:51], v[80:81]
	v_pk_add_f32 v[66:67], v[66:67], v[68:69]
	v_pk_add_f32 v[68:69], v[70:71], v[72:73]
	v_pk_add_f32 v[70:71], v[74:75], v[76:77]
	v_pk_add_f32 v[72:73], v[80:81], v[78:79]
	v_pk_add_f32 v[68:69], v[70:71], v[68:69]
	v_pk_add_f32 v[66:67], v[72:73], v[66:67]
	v_pk_mul_f32 v[72:73], v[14:15], v[14:15]
	v_pk_mov_b32 v[70:71], v[66:67], v[68:69] op_sel:[1,0]
	v_mov_b32_e32 v67, v69
	v_pk_add_f32 v[66:67], v[70:71], v[66:67]
	v_pk_mul_f32 v[70:71], v[6:7], v[6:7]
	v_pk_mul_f32 v[74:75], v[8:9], v[8:9]
	v_pk_mul_f32 v[76:77], v[16:17], v[16:17]
	v_pk_mul_f32 v[78:79], v[4:5], v[4:5]
	v_pk_mul_f32 v[80:81], v[12:13], v[12:13]
	v_pk_mul_f32 v[82:83], v[10:11], v[10:11]
	v_pk_mul_f32 v[84:85], v[2:3], v[2:3]
	v_pk_fma_f32 v[82:83], v[42:43], v[42:43], v[82:83]
	v_pk_fma_f32 v[80:81], v[44:45], v[44:45], v[80:81]
	v_pk_fma_f32 v[78:79], v[36:37], v[36:37], v[78:79]
	v_pk_fma_f32 v[76:77], v[48:49], v[48:49], v[76:77]
	v_pk_fma_f32 v[74:75], v[40:41], v[40:41], v[74:75]
	v_pk_fma_f32 v[72:73], v[46:47], v[46:47], v[72:73]
	v_pk_fma_f32 v[70:71], v[38:39], v[38:39], v[70:71]
	v_pk_fma_f32 v[84:85], v[34:35], v[34:35], v[84:85]
	v_pk_add_f32 v[70:71], v[70:71], v[72:73]
	v_pk_add_f32 v[72:73], v[74:75], v[76:77]
	v_pk_add_f32 v[74:75], v[78:79], v[80:81]
	v_pk_add_f32 v[76:77], v[84:85], v[82:83]
	v_pk_add_f32 v[72:73], v[74:75], v[72:73]
	v_pk_add_f32 v[70:71], v[76:77], v[70:71]
	v_pk_add_f32 v[66:67], v[66:67], v[66:67] op_sel:[0,1] op_sel_hi:[1,0]
	v_add_f32_e32 v70, v71, v70
	v_add_f32_e32 v71, v72, v73
	v_mov_b32_e32 v69, v66
	v_add_f32_e32 v70, v70, v71
	s_nop 0
	v_permlane32_swap_b32_e32 v66, v69
	v_mov_b32_e32 v68, v70
	s_nop 1
	v_permlane32_swap_b32_e32 v70, v68
	v_mov_b32_e32 v71, v66
	v_pk_add_f32 v[66:67], v[70:71], v[68:69]
	v_pk_fma_f32 v[66:67], v[66:67], s[0:1], v[152:153] op_sel_hi:[1,0,0]
	s_mov_b32 s1, 0x800000
	v_rsq_f32_e32 v68, v67
	s_nop 0
	v_pk_mul_f32 v[158:159], v[50:51], v[68:69] op_sel_hi:[1,0]
	v_pk_mul_f32 v[50:51], v[18:19], v[68:69] op_sel_hi:[1,0]
	v_pk_mul_f32 v[80:81], v[60:61], v[68:69] op_sel_hi:[1,0]
	v_pk_mul_f32 v[60:61], v[28:29], v[68:69] op_sel_hi:[1,0]
	v_pk_mul_f32 v[78:79], v[58:59], v[68:69] op_sel_hi:[1,0]
	v_pk_mul_f32 v[160:161], v[52:53], v[68:69] op_sel_hi:[1,0]
	v_pk_mul_f32 v[82:83], v[54:55], v[68:69] op_sel_hi:[1,0]
	v_rsq_f32_e32 v28, v66
	v_pk_mul_f32 v[168:169], v[56:57], v[68:69] op_sel_hi:[1,0]
	v_pk_mul_f32 v[58:59], v[26:27], v[68:69] op_sel_hi:[1,0]
	v_pk_mul_f32 v[52:53], v[20:21], v[68:69] op_sel_hi:[1,0]
	v_pk_mul_f32 v[54:55], v[22:23], v[68:69] op_sel_hi:[1,0]
	v_pk_mul_f32 v[56:57], v[24:25], v[68:69] op_sel_hi:[1,0]
	v_pk_mul_f32 v[18:19], v[42:43], v[28:29] op_sel_hi:[1,0]
	v_pk_mul_f32 v[20:21], v[44:45], v[28:29] op_sel_hi:[1,0]
	v_pk_mul_f32 v[22:23], v[46:47], v[28:29] op_sel_hi:[1,0]
	v_pk_mul_f32 v[26:27], v[48:49], v[28:29] op_sel_hi:[1,0]
	v_pk_mul_f32 v[162:163], v[34:35], v[28:29] op_sel_hi:[1,0]
	v_pk_mul_f32 v[164:165], v[36:37], v[28:29] op_sel_hi:[1,0]
	v_pk_mul_f32 v[166:167], v[38:39], v[28:29] op_sel_hi:[1,0]
	v_pk_mul_f32 v[24:25], v[40:41], v[28:29] op_sel_hi:[1,0]
	v_pk_mul_f32 v[104:105], v[2:3], v[28:29] op_sel_hi:[1,0]
	v_pk_mul_f32 v[112:113], v[4:5], v[28:29] op_sel_hi:[1,0]
	ds_read_b128 v[2:5], v150 offset:60416
	ds_read_b128 v[34:37], v174 offset:32768
	ds_read_b128 v[38:41], v174 offset:32800
	ds_read_b128 v[42:45], v174 offset:32832
	ds_read_b128 v[46:49], v174 offset:32864
	v_cvt_pk_bf16_f32 v129, v168, v169
	v_cvt_pk_bf16_f32 v128, v82, v83
	v_cvt_pk_bf16_f32 v127, v160, v161
	v_cvt_pk_bf16_f32 v126, v158, v159
	v_cvt_pk_bf16_f32 v137, v24, v25
	v_cvt_pk_bf16_f32 v136, v166, v167
	v_cvt_pk_bf16_f32 v135, v164, v165
	s_waitcnt lgkmcnt(0)
	v_mfma_f32_32x32x16_bf16 v[86:101], v[2:5], v[126:129], v[34:49]
	v_cvt_pk_bf16_f32 v134, v162, v163
	v_mul_f32_e32 v84, v62, v68
	v_mul_f32_e32 v85, v63, v68
	v_mul_f32_e32 v170, v64, v68
	v_mul_f32_e32 v171, v65, v68
	v_pk_mul_f32 v[62:63], v[30:31], v[68:69] op_sel_hi:[1,0]
	v_pk_mul_f32 v[64:65], v[32:33], v[68:69] op_sel_hi:[1,0]
	v_pk_mul_f32 v[116:117], v[6:7], v[28:29] op_sel_hi:[1,0]
	v_pk_mul_f32 v[154:155], v[8:9], v[28:29] op_sel_hi:[1,0]
	v_mfma_f32_32x32x16_bf16 v[34:49], v[2:5], v[134:137], v[34:49]
	ds_read_b128 v[6:9], v150 offset:61440
	ds_read_b128 v[66:69], v174 offset:32896
	ds_read_b128 v[106:109], v150 offset:64512
	v_cvt_pk_bf16_f32 v125, v170, v171
	v_cvt_pk_bf16_f32 v124, v84, v85
	v_cvt_pk_bf16_f32 v123, v80, v81
	v_cvt_pk_bf16_f32 v122, v78, v79
	v_cvt_pk_bf16_f32 v149, v26, v27
	v_cvt_pk_bf16_f32 v148, v22, v23
	v_cvt_pk_bf16_f32 v147, v20, v21
	v_cvt_pk_bf16_f32 v146, v18, v19
	s_waitcnt lgkmcnt(2)
	v_mfma_f32_32x32x16_bf16 v[86:101], v[6:9], v[122:125], v[86:101]
	v_mul_f32_e32 v102, v10, v28
	v_mul_f32_e32 v103, v11, v28
	v_mul_f32_e32 v110, v12, v28
	v_mul_f32_e32 v111, v13, v28
	v_mul_f32_e32 v114, v14, v28
	v_mul_f32_e32 v115, v15, v28
	v_pk_mul_f32 v[156:157], v[16:17], v[28:29] op_sel_hi:[1,0]
	ds_read_b128 v[176:179], v174 offset:33536
	ds_read_b128 v[180:183], v174 offset:33568
	ds_read_b128 v[184:187], v174 offset:33600
	ds_read_b128 v[28:31], v174 offset:33632
	ds_read_b128 v[188:191], v174 offset:33792
	ds_read_b128 v[192:195], v174 offset:33824
	ds_read_b128 v[196:199], v174 offset:33856
	ds_read_b128 v[200:203], v174 offset:33888
	ds_read_b128 v[204:207], v150 offset:62464
	v_cvt_pk_bf16_f32 v133, v56, v57
	v_mfma_f32_32x32x16_bf16 v[34:49], v[6:9], v[146:149], v[34:49]
	v_cvt_pk_bf16_f32 v132, v54, v55
	v_cvt_pk_bf16_f32 v131, v52, v53
	v_cvt_pk_bf16_f32 v130, v50, v51
	ds_read_b128 v[70:73], v174 offset:33664
	ds_read_b128 v[74:77], v174 offset:33920
	ds_read_b128 v[208:211], v150 offset:63488
	v_cvt_pk_bf16_f32 v145, v154, v155
	v_cvt_pk_bf16_f32 v144, v116, v117
	v_cvt_pk_bf16_f32 v143, v112, v113
	v_cvt_pk_bf16_f32 v142, v104, v105
	s_waitcnt lgkmcnt(3)
	v_mfma_f32_32x32x16_bf16 v[86:101], v[204:207], v[130:133], v[86:101]
	v_cvt_pk_bf16_f32 v121, v64, v65
	v_cvt_pk_bf16_f32 v120, v62, v63
	v_cvt_pk_bf16_f32 v119, v60, v61
	v_cvt_pk_bf16_f32 v118, v58, v59
	v_cvt_pk_bf16_f32 v141, v156, v157
	v_cvt_pk_bf16_f32 v140, v114, v115
	v_cvt_pk_bf16_f32 v139, v110, v111
	v_mfma_f32_32x32x16_bf16 v[34:49], v[204:207], v[142:145], v[34:49]
	v_cvt_pk_bf16_f32 v138, v102, v103
	v_fma_f32 v16, v30, v170, v202
	v_fma_f32 v17, v31, v171, v203
	v_fma_f32 v14, v28, v84, v200
	v_fma_f32 v15, v29, v85, v201
	v_pk_fma_f32 v[12:13], v[186:187], v[80:81], v[198:199]
	v_pk_fma_f32 v[10:11], v[184:185], v[78:79], v[196:197]
	v_pk_fma_f32 v[8:9], v[182:183], v[168:169], v[194:195]
	s_waitcnt lgkmcnt(0)
	v_mfma_f32_32x32x16_bf16 v[86:101], v[208:211], v[118:121], v[86:101]
	v_fma_f32 v6, v180, v82, v192
	v_fma_f32 v7, v181, v83, v193
	ds_read_b128 v[78:81], v174 offset:33760
	ds_read_b128 v[82:85], v174 offset:33248
	v_fma_f32 v4, v178, v160, v190
	v_fma_f32 v5, v179, v161, v191
	v_pk_fma_f32 v[2:3], v[176:177], v[158:159], v[188:189]
	v_pk_fma_f32 v[32:33], v[30:31], v[26:27], v[202:203]
	v_pk_fma_f32 v[30:31], v[28:29], v[22:23], v[200:201]
	v_pk_fma_f32 v[28:29], v[186:187], v[20:21], v[198:199]
	v_pk_fma_f32 v[26:27], v[184:185], v[18:19], v[196:197]
	v_pk_fma_f32 v[24:25], v[182:183], v[24:25], v[194:195]
	v_pk_fma_f32 v[22:23], v[180:181], v[166:167], v[192:193]
	v_pk_fma_f32 v[20:21], v[178:179], v[164:165], v[190:191]
	v_pk_fma_f32 v[18:19], v[176:177], v[162:163], v[188:189]
	ds_read_b128 v[158:161], v174 offset:33696
	ds_read_b128 v[162:165], v174 offset:33728
	ds_read_b128 v[166:169], v174 offset:33952
	ds_read_b128 v[176:179], v174 offset:33984
	ds_read_b128 v[180:183], v174 offset:34016
	ds_read_b128 v[184:187], v212 offset:11264
	v_mfma_f32_32x32x16_bf16 v[34:49], v[208:211], v[138:141], v[34:49]
	v_cvt_pk_bf16_f32 v86, v86, v87
	v_cvt_pk_bf16_f32 v87, v88, v89
	v_cvt_pk_bf16_f32 v88, v90, v91
	v_cvt_pk_bf16_f32 v89, v92, v93
	ds_read_b128 v[90:93], v212 offset:12288
	v_pk_max_i16 v86, v86, 0
	v_pk_max_i16 v87, v87, 0
	v_pk_max_i16 v88, v88, 0
	v_pk_max_i16 v89, v89, 0
	s_nop 1
	s_nop 0
	v_cvt_pk_bf16_f32 v188, v34, v35
	v_cvt_pk_bf16_f32 v189, v36, v37
	v_cvt_pk_bf16_f32 v190, v38, v39
	v_cvt_pk_bf16_f32 v191, v40, v41
	s_waitcnt lgkmcnt(1)
	v_mfma_f32_32x32x16_bf16 v[2:17], v[184:187], v[86:89], v[2:17]
	v_pk_max_i16 v188, v188, 0
	v_pk_max_i16 v189, v189, 0
	v_pk_max_i16 v190, v190, 0
	v_pk_max_i16 v191, v191, 0
	v_cvt_pk_bf16_f32 v94, v94, v95
	v_cvt_pk_bf16_f32 v95, v96, v97
	v_cvt_pk_bf16_f32 v96, v98, v99
	v_cvt_pk_bf16_f32 v97, v100, v101
	v_cvt_pk_bf16_f32 v98, v42, v43
	v_cvt_pk_bf16_f32 v99, v44, v45
	v_mfma_f32_32x32x16_bf16 v[18:33], v[184:187], v[188:191], v[18:33]
	ds_read_b128 v[184:187], v212 offset:19456
	v_cvt_pk_bf16_f32 v100, v46, v47
	v_cvt_pk_bf16_f32 v101, v48, v49
	v_fma_f32 v64, v80, v64, v182
	v_fma_f32 v65, v81, v65, v183
	v_pk_fma_f32 v[62:63], v[78:79], v[62:63], v[180:181]
	v_pk_fma_f32 v[60:61], v[164:165], v[60:61], v[178:179]
	v_pk_fma_f32 v[58:59], v[162:163], v[58:59], v[176:177]
	v_pk_max_i16 v94, v94, 0
	v_pk_max_i16 v95, v95, 0
	v_pk_max_i16 v96, v96, 0
	v_pk_max_i16 v97, v97, 0
	v_pk_max_i16 v98, v98, 0
	v_pk_max_i16 v99, v99, 0
	v_pk_max_i16 v100, v100, 0
	v_pk_max_i16 v101, v101, 0
	v_pk_fma_f32 v[56:57], v[160:161], v[56:57], v[168:169]
	s_waitcnt lgkmcnt(1)
	v_mfma_f32_32x32x16_bf16 v[2:17], v[90:93], v[94:97], v[2:17]
	v_fma_f32 v54, v158, v54, v166
	v_fma_f32 v55, v159, v55, v167
	v_fma_f32 v52, v72, v52, v76
	v_fma_f32 v53, v73, v53, v77
	v_fma_f32 v50, v70, v50, v74
	v_fma_f32 v51, v71, v51, v75
	v_pk_fma_f32 v[48:49], v[80:81], v[156:157], v[182:183]
	v_pk_fma_f32 v[46:47], v[78:79], v[114:115], v[180:181]
	v_pk_fma_f32 v[44:45], v[164:165], v[110:111], v[178:179]
	v_pk_fma_f32 v[42:43], v[162:163], v[102:103], v[176:177]
	v_mfma_f32_32x32x16_bf16 v[18:33], v[90:93], v[98:101], v[18:33]
	ds_read_b128 v[90:93], v212 offset:20480
	v_fma_f32 v40, v160, v154, v168
	v_fma_f32 v41, v161, v155, v169
	v_fma_f32 v38, v158, v116, v166
	v_fma_f32 v39, v159, v117, v167
	v_pk_fma_f32 v[36:37], v[72:73], v[112:113], v[76:77]
	v_pk_fma_f32 v[34:35], v[70:71], v[104:105], v[74:75]
	s_waitcnt lgkmcnt(1)
	v_mfma_f32_32x32x16_bf16 v[50:65], v[184:187], v[86:89], v[50:65]
	ds_read_b128 v[70:73], v174 offset:32928
	ds_read_b128 v[74:77], v174 offset:32960
	ds_read_b128 v[78:81], v174 offset:32992
	ds_read_b128 v[86:89], v174 offset:33024
	ds_read_b128 v[110:113], v212 offset:1024
	v_mfma_f32_32x32x16_bf16 v[34:49], v[184:187], v[188:191], v[34:49]
	s_waitcnt lgkmcnt(5)
	v_mfma_f32_32x32x16_bf16 v[50:65], v[90:93], v[94:97], v[50:65]
	v_mfma_f32_32x32x16_bf16 v[34:49], v[90:93], v[98:101], v[34:49]
	s_waitcnt lgkmcnt(2)
	v_mfma_f32_32x32x16_bf16 v[90:105], v[106:109], v[126:129], v[66:81]
	v_mfma_f32_32x32x16_bf16 v[66:81], v[106:109], v[134:137], v[66:81]
	ds_read_b128 v[106:109], v212 offset:0
	s_waitcnt lgkmcnt(0)
	v_mfma_f32_32x32x16_bf16 v[90:105], v[106:109], v[122:125], v[90:105]
	v_mfma_f32_32x32x16_bf16 v[66:81], v[106:109], v[146:149], v[66:81]
	ds_read_b128 v[106:109], v212 offset:2048
	v_mfma_f32_32x32x16_bf16 v[90:105], v[110:113], v[130:133], v[90:105]
	v_mfma_f32_32x32x16_bf16 v[66:81], v[110:113], v[142:145], v[66:81]
	ds_read_b128 v[110:113], v212 offset:13312
	s_waitcnt lgkmcnt(1)
	v_mfma_f32_32x32x16_bf16 v[90:105], v[106:109], v[118:121], v[90:105]
	v_mfma_f32_32x32x16_bf16 v[66:81], v[106:109], v[138:141], v[66:81]
	s_nop 10
	v_cvt_pk_bf16_f32 v90, v90, v91
	v_cvt_pk_bf16_f32 v91, v92, v93
	v_cvt_pk_bf16_f32 v92, v94, v95
	v_cvt_pk_bf16_f32 v94, v98, v99
	v_cvt_pk_bf16_f32 v95, v100, v101
	ds_read_b128 v[98:101], v212 offset:21504
	v_cvt_pk_bf16_f32 v66, v66, v67
	v_cvt_pk_bf16_f32 v67, v68, v69
	v_cvt_pk_bf16_f32 v68, v70, v71
	v_cvt_pk_bf16_f32 v93, v96, v97
	v_cvt_pk_bf16_f32 v69, v72, v73
	ds_read_b128 v[70:73], v212 offset:14336
	v_pk_max_i16 v90, v90, 0
	v_pk_max_i16 v91, v91, 0
	v_pk_max_i16 v92, v92, 0
	v_pk_max_i16 v93, v93, 0
	v_pk_max_i16 v66, v66, 0
	v_pk_max_i16 v67, v67, 0
	v_pk_max_i16 v68, v68, 0
	v_pk_max_i16 v69, v69, 0
	v_cvt_pk_bf16_f32 v96, v102, v103
	s_waitcnt lgkmcnt(2)
	v_mfma_f32_32x32x16_bf16 v[2:17], v[110:113], v[90:93], v[2:17]
	v_cvt_pk_bf16_f32 v97, v104, v105
	v_cvt_pk_bf16_f32 v74, v74, v75
	v_cvt_pk_bf16_f32 v75, v76, v77
	v_cvt_pk_bf16_f32 v76, v78, v79
	v_cvt_pk_bf16_f32 v77, v80, v81
	v_pk_max_i16 v94, v94, 0
	v_pk_max_i16 v95, v95, 0
	v_pk_max_i16 v96, v96, 0
	v_pk_max_i16 v97, v97, 0
	v_pk_max_i16 v74, v74, 0
	v_pk_max_i16 v75, v75, 0
	v_pk_max_i16 v76, v76, 0
	v_pk_max_i16 v77, v77, 0
	v_mfma_f32_32x32x16_bf16 v[18:33], v[110:113], v[66:69], v[18:33]
	s_waitcnt lgkmcnt(1)
	v_mfma_f32_32x32x16_bf16 v[34:49], v[98:101], v[66:69], v[34:49]
	ds_read_b128 v[66:69], v212 offset:22528
	v_mfma_f32_32x32x16_bf16 v[50:65], v[98:101], v[90:93], v[50:65]
	s_waitcnt lgkmcnt(1)
	v_mfma_f32_32x32x16_bf16 v[2:17], v[70:73], v[94:97], v[2:17]
	v_mfma_f32_32x32x16_bf16 v[18:33], v[70:73], v[74:77], v[18:33]
	ds_read_b128 v[78:81], v212 offset:3072
	s_waitcnt lgkmcnt(1)
	v_mfma_f32_32x32x16_bf16 v[50:65], v[66:69], v[94:97], v[50:65]
	ds_read_b128 v[90:93], v174 offset:33056
	ds_read_b128 v[94:97], v174 offset:33088
	ds_read_b128 v[98:101], v174 offset:33120
	ds_read_b128 v[70:73], v174 offset:33152
	v_mfma_f32_32x32x16_bf16 v[34:49], v[66:69], v[74:77], v[34:49]
	ds_read_b128 v[66:69], v212 offset:4096
	ds_read_b128 v[74:77], v212 offset:5120
	s_waitcnt lgkmcnt(3)
	v_mfma_f32_32x32x16_bf16 v[102:117], v[78:81], v[126:129], v[86:101]
	v_mfma_f32_32x32x16_bf16 v[86:101], v[78:81], v[134:137], v[86:101]
	s_waitcnt lgkmcnt(1)
	v_mfma_f32_32x32x16_bf16 v[86:101], v[66:69], v[146:149], v[86:101]
	v_mfma_f32_32x32x16_bf16 v[102:117], v[66:69], v[122:125], v[102:117]
	ds_read_b128 v[66:69], v212 offset:6144
	s_waitcnt lgkmcnt(1)
	v_mfma_f32_32x32x16_bf16 v[86:101], v[74:77], v[142:145], v[86:101]
	v_mfma_f32_32x32x16_bf16 v[102:117], v[74:77], v[130:133], v[102:117]
	ds_read_b128 v[74:77], v212 offset:15360
	s_waitcnt lgkmcnt(1)
	v_mfma_f32_32x32x16_bf16 v[86:101], v[66:69], v[138:141], v[86:101]
	v_mfma_f32_32x32x16_bf16 v[102:117], v[66:69], v[118:121], v[102:117]
	s_nop 10
	v_cvt_pk_bf16_f32 v78, v86, v87
	v_cvt_pk_bf16_f32 v80, v90, v91
	v_cvt_pk_bf16_f32 v79, v88, v89
	v_cvt_pk_bf16_f32 v81, v92, v93
	ds_read_b128 v[86:89], v212 offset:16384
	ds_read_b128 v[90:93], v212 offset:23552
	v_cvt_pk_bf16_f32 v66, v102, v103
	v_cvt_pk_bf16_f32 v67, v104, v105
	v_cvt_pk_bf16_f32 v68, v106, v107
	v_cvt_pk_bf16_f32 v69, v108, v109
	v_pk_max_i16 v66, v66, 0
	v_pk_max_i16 v67, v67, 0
	v_pk_max_i16 v68, v68, 0
	v_pk_max_i16 v69, v69, 0
	v_pk_max_i16 v78, v78, 0
	v_pk_max_i16 v79, v79, 0
	v_pk_max_i16 v80, v80, 0
	v_pk_max_i16 v81, v81, 0
	v_cvt_pk_bf16_f32 v94, v94, v95
	s_waitcnt lgkmcnt(2)
	v_mfma_f32_32x32x16_bf16 v[18:33], v[74:77], v[78:81], v[18:33]
	v_cvt_pk_bf16_f32 v95, v96, v97
	v_cvt_pk_bf16_f32 v96, v98, v99
	v_cvt_pk_bf16_f32 v97, v100, v101
	v_pk_max_i16 v94, v94, 0
	v_pk_max_i16 v95, v95, 0
	v_pk_max_i16 v96, v96, 0
	v_pk_max_i16 v97, v97, 0
	v_mfma_f32_32x32x16_bf16 v[2:17], v[74:77], v[66:69], v[2:17]
	v_cvt_pk_bf16_f32 v74, v110, v111
	v_cvt_pk_bf16_f32 v75, v112, v113
	v_cvt_pk_bf16_f32 v76, v114, v115
	v_cvt_pk_bf16_f32 v77, v116, v117
	v_pk_max_i16 v74, v74, 0
	v_pk_max_i16 v75, v75, 0
	v_pk_max_i16 v76, v76, 0
	v_pk_max_i16 v77, v77, 0
	s_waitcnt lgkmcnt(0)
	v_mfma_f32_32x32x16_bf16 v[50:65], v[90:93], v[66:69], v[50:65]
	ds_read_b128 v[66:69], v212 offset:24576
	v_mfma_f32_32x32x16_bf16 v[34:49], v[90:93], v[78:81], v[34:49]
	ds_read_b128 v[102:105], v212 offset:7168
	v_mfma_f32_32x32x16_bf16 v[2:17], v[86:89], v[74:77], v[2:17]
	s_waitcnt lgkmcnt(1)
	v_mfma_f32_32x32x16_bf16 v[50:65], v[66:69], v[74:77], v[50:65]
	ds_read_b128 v[74:77], v174 offset:33184
	ds_read_b128 v[78:81], v174 offset:33216
	v_mfma_f32_32x32x16_bf16 v[34:49], v[66:69], v[94:97], v[34:49]
	ds_read_b128 v[66:69], v212 offset:8192
	v_mfma_f32_32x32x16_bf16 v[18:33], v[86:89], v[94:97], v[18:33]
	s_waitcnt lgkmcnt(1)
	v_mfma_f32_32x32x16_bf16 v[86:101], v[102:105], v[126:129], v[70:85]
	v_mfma_f32_32x32x16_bf16 v[70:85], v[102:105], v[134:137], v[70:85]
	ds_read_b128 v[102:105], v212 offset:9216
	v_lshlrev_b32_e32 v135, 2, v1
	v_add_u32_e32 v134, v172, v174
	s_waitcnt lgkmcnt(1)
	v_mfma_f32_32x32x16_bf16 v[86:101], v[66:69], v[122:125], v[86:101]
	v_mfma_f32_32x32x16_bf16 v[70:85], v[66:69], v[146:149], v[70:85]
	ds_read_b128 v[66:69], v212 offset:10240
	s_waitcnt lgkmcnt(1)
	v_mfma_f32_32x32x16_bf16 v[86:101], v[102:105], v[130:133], v[86:101]
	v_mfma_f32_32x32x16_bf16 v[70:85], v[102:105], v[142:145], v[70:85]
	ds_read_b128 v[102:105], v212 offset:17408
	s_waitcnt lgkmcnt(1)
	v_mfma_f32_32x32x16_bf16 v[86:101], v[66:69], v[118:121], v[86:101]
	v_mfma_f32_32x32x16_bf16 v[70:85], v[66:69], v[138:141], v[70:85]
	s_nop 10
	v_cvt_pk_bf16_f32 v68, v90, v91
	v_cvt_pk_bf16_f32 v69, v92, v93
	ds_read_b128 v[90:93], v212 offset:25600
	v_cvt_pk_bf16_f32 v66, v86, v87
	v_cvt_pk_bf16_f32 v67, v88, v89
	v_pk_max_i16 v66, v66, 0
	v_pk_max_i16 v67, v67, 0
	v_pk_max_i16 v68, v68, 0
	v_pk_max_i16 v69, v69, 0
	v_cvt_pk_bf16_f32 v70, v70, v71
	v_cvt_pk_bf16_f32 v71, v72, v73
	s_waitcnt lgkmcnt(1)
	v_mfma_f32_32x32x16_bf16 v[2:17], v[102:105], v[66:69], v[2:17]
	v_cvt_pk_bf16_f32 v72, v74, v75
	v_cvt_pk_bf16_f32 v73, v76, v77
	ds_read_b128 v[74:77], v212 offset:18432
	v_cvt_pk_bf16_f32 v86, v94, v95
	v_cvt_pk_bf16_f32 v87, v96, v97
	v_cvt_pk_bf16_f32 v88, v98, v99
	s_waitcnt lgkmcnt(1)
	v_mfma_f32_32x32x16_bf16 v[50:65], v[90:93], v[66:69], v[50:65]
	ds_read_b128 v[66:69], v212 offset:26624
	v_cvt_pk_bf16_f32 v89, v100, v101
	v_pk_max_i16 v86, v86, 0
	v_pk_max_i16 v87, v87, 0
	v_pk_max_i16 v88, v88, 0
	v_pk_max_i16 v89, v89, 0
	v_pk_max_i16 v70, v70, 0
	v_pk_max_i16 v71, v71, 0
	v_pk_max_i16 v72, v72, 0
	v_pk_max_i16 v73, v73, 0
	v_cvt_pk_bf16_f32 v78, v78, v79
	v_cvt_pk_bf16_f32 v79, v80, v81
	s_waitcnt lgkmcnt(1)
	v_mfma_f32_32x32x16_bf16 v[2:17], v[74:77], v[86:89], v[2:17]
	v_cvt_pk_bf16_f32 v80, v82, v83
	v_cvt_pk_bf16_f32 v81, v84, v85
	v_pk_max_i16 v78, v78, 0
	v_pk_max_i16 v79, v79, 0
	v_pk_max_i16 v80, v80, 0
	v_pk_max_i16 v81, v81, 0
	s_waitcnt lgkmcnt(0)
	v_mfma_f32_32x32x16_bf16 v[50:65], v[66:69], v[86:89], v[50:65]
	v_mfma_f32_32x32x16_bf16 v[34:49], v[90:93], v[70:73], v[34:49]
	s_nop 10
	v_add_f32_e32 v130, v10, v58
	v_add_f32_e32 v131, v11, v59
	v_add_f32_e32 v132, v12, v60
	v_add_f32_e32 v133, v13, v61
	v_add_f32_e32 v138, v4, v52
	v_add_f32_e32 v139, v5, v53
	v_pk_add_f32 v[140:141], v[16:17], v[64:65]
	v_pk_add_f32 v[142:143], v[8:9], v[56:57]
	v_pk_add_f32 v[144:145], v[14:15], v[62:63]
	v_pk_add_f32 v[146:147], v[6:7], v[54:55]
	v_mfma_f32_32x32x16_bf16 v[18:33], v[102:105], v[70:73], v[18:33]
	ds_read2st64_b32 v[70:71], v135 offset0:133 offset1:134
	v_add_f32_e32 v148, v2, v50
	v_add_f32_e32 v149, v3, v51
	v_add_f32_e32 v144, v146, v144
	v_add_f32_e32 v145, v147, v145
	v_pk_add_f32 v[140:141], v[142:143], v[140:141]
	v_pk_add_f32 v[132:133], v[138:139], v[132:133]
	v_pk_add_f32 v[130:131], v[148:149], v[130:131]
	v_pk_add_f32 v[132:133], v[132:133], v[140:141]
	v_pk_add_f32 v[130:131], v[130:131], v[144:145]
	v_mfma_f32_32x32x16_bf16 v[34:49], v[66:69], v[78:81], v[34:49]
	s_waitcnt vmcnt(0) lgkmcnt(0)
	v_mul_f32_e32 v66, v175, v70
	v_add_f32_e32 v130, v131, v130
	v_add_f32_e32 v131, v132, v133
	ds_write_b32 v173, v66 offset:512
	v_mul_f32_e32 v66, v175, v71
	v_add_f32_e32 v130, v130, v131
	s_waitcnt lgkmcnt(0)
	ds_read_b128 v[102:105], v174 offset:34560
	ds_read_b128 v[98:101], v174 offset:34592
	ds_read_b128 v[110:113], v174 offset:34624
	ds_read_b128 v[106:109], v174 offset:34656
	ds_read_b128 v[114:117], v174 offset:34688
	ds_read_b128 v[122:125], v174 offset:34720
	ds_read_b128 v[118:121], v174 offset:34752
	ds_read_b128 v[126:129], v174 offset:34784
	v_mov_b32_dpp v66, v66 quad_perm:[1,0,3,2] row_mask:0xf bank_mask:0xf bound_ctrl:1
	v_mov_b32_e32 v131, v130
	v_fmac_f32_e32 v66, v175, v71
	s_nop 0
	v_permlane32_swap_b32_e32 v130, v131
	v_add_f32_dpp v66, v66, v66 quad_perm:[2,3,0,1] row_mask:0xf bank_mask:0xf bound_ctrl:1
	v_add_f32_e32 v130, v130, v131
	v_fmamk_f32 v65, v130, 0xbc800000, v65
	v_add_f32_dpp v66, v66, v66 row_half_mirror row_mask:0xf bank_mask:0xf bound_ctrl:1
	v_fmamk_f32 v64, v130, 0xbc800000, v64
	v_fmamk_f32 v63, v130, 0xbc800000, v63
	v_fmamk_f32 v62, v130, 0xbc800000, v62
	v_fmamk_f32 v61, v130, 0xbc800000, v61
	v_fmamk_f32 v60, v130, 0xbc800000, v60
	v_fmamk_f32 v59, v130, 0xbc800000, v59
	v_fmamk_f32 v58, v130, 0xbc800000, v58
	v_fmamk_f32 v57, v130, 0xbc800000, v57
	v_fmamk_f32 v56, v130, 0xbc800000, v56
	v_fmamk_f32 v55, v130, 0xbc800000, v55
	v_fmamk_f32 v54, v130, 0xbc800000, v54
	v_fmamk_f32 v53, v130, 0xbc800000, v53
	v_fmamk_f32 v52, v130, 0xbc800000, v52
	v_fmamk_f32 v51, v130, 0xbc800000, v51
	v_fmac_f32_e32 v50, 0xbc800000, v130
	v_add_f32_dpp v66, v66, v66 row_ror:8 row_mask:0xf bank_mask:0xf bound_ctrl:1
	v_fmamk_f32 v17, v130, 0xbc800000, v17
	v_fmamk_f32 v16, v130, 0xbc800000, v16
	v_fmamk_f32 v15, v130, 0xbc800000, v15
	v_fmamk_f32 v14, v130, 0xbc800000, v14
	v_fmamk_f32 v13, v130, 0xbc800000, v13
	v_fmamk_f32 v12, v130, 0xbc800000, v12
	v_fmamk_f32 v11, v130, 0xbc800000, v11
	v_fmamk_f32 v10, v130, 0xbc800000, v10
	v_fmamk_f32 v9, v130, 0xbc800000, v9
	v_fmamk_f32 v8, v130, 0xbc800000, v8
	v_fmamk_f32 v7, v130, 0xbc800000, v7
	v_fmamk_f32 v6, v130, 0xbc800000, v6
	v_fmamk_f32 v5, v130, 0xbc800000, v5
	v_fmamk_f32 v4, v130, 0xbc800000, v4
	v_fmamk_f32 v3, v130, 0xbc800000, v3
	v_fmac_f32_e32 v2, 0xbc800000, v130
	v_pk_mul_f32 v[130:131], v[54:55], v[54:55]
	v_pk_mul_f32 v[132:133], v[62:63], v[62:63]
	v_pk_mul_f32 v[138:139], v[50:51], v[50:51]
	v_pk_mul_f32 v[140:141], v[58:59], v[58:59]
	v_pk_mul_f32 v[142:143], v[56:57], v[56:57]
	v_pk_mul_f32 v[144:145], v[64:65], v[64:65]
	v_pk_mul_f32 v[146:147], v[52:53], v[52:53]
	v_pk_mul_f32 v[148:149], v[60:61], v[60:61]
	v_mov_b32_e32 v67, v66
	v_pk_fma_f32 v[148:149], v[12:13], v[12:13], v[148:149]
	v_pk_fma_f32 v[146:147], v[4:5], v[4:5], v[146:147]
	v_pk_fma_f32 v[144:145], v[16:17], v[16:17], v[144:145]
	v_pk_fma_f32 v[142:143], v[8:9], v[8:9], v[142:143]
	v_pk_fma_f32 v[140:141], v[10:11], v[10:11], v[140:141]
	v_pk_fma_f32 v[138:139], v[2:3], v[2:3], v[138:139]
	v_pk_fma_f32 v[132:133], v[14:15], v[14:15], v[132:133]
	v_pk_fma_f32 v[130:131], v[6:7], v[6:7], v[130:131]
	v_permlane16_swap_b32_e32 v66, v67
	v_pk_add_f32 v[130:131], v[130:131], v[132:133]
	v_pk_add_f32 v[132:133], v[138:139], v[140:141]
	v_pk_add_f32 v[138:139], v[142:143], v[144:145]
	v_pk_add_f32 v[140:141], v[146:147], v[148:149]
	v_mfma_f32_32x32x16_bf16 v[18:33], v[74:77], v[78:81], v[18:33]
	v_add_f32_e32 v136, v66, v67
	ds_read_b128 v[70:73], v134 offset:512
	ds_read_b128 v[66:69], v134 offset:544
	ds_read_b128 v[78:81], v134 offset:576
	ds_read_b128 v[74:77], v134 offset:608
	ds_read_b128 v[82:85], v134 offset:640
	ds_read_b128 v[90:93], v134 offset:672
	ds_read_b128 v[86:89], v134 offset:704
	ds_read_b128 v[94:97], v134 offset:736
	v_pk_add_f32 v[138:139], v[140:141], v[138:139]
	v_pk_add_f32 v[130:131], v[132:133], v[130:131]
	s_waitcnt lgkmcnt(8)
	v_pk_mul_f32 v[140:141], v[126:127], v[62:63]
	v_pk_mov_b32 v[132:133], v[130:131], v[138:139] op_sel:[1,0]
	v_mov_b32_e32 v131, v139
	v_pk_mul_f32 v[138:139], v[122:123], v[54:55]
	v_pk_mul_f32 v[142:143], v[114:115], v[50:51]
	v_pk_mul_f32 v[144:145], v[118:119], v[58:59]
	v_pk_mul_f32 v[146:147], v[124:125], v[56:57]
	v_pk_mul_f32 v[148:149], v[128:129], v[64:65]
	v_pk_mul_f32 v[154:155], v[116:117], v[52:53]
	v_pk_mul_f32 v[156:157], v[120:121], v[60:61]
	v_pk_fma_f32 v[154:155], v[104:105], v[4:5], v[154:155]
	v_pk_fma_f32 v[156:157], v[112:113], v[12:13], v[156:157]
	v_pk_fma_f32 v[148:149], v[108:109], v[16:17], v[148:149]
	v_pk_fma_f32 v[146:147], v[100:101], v[8:9], v[146:147]
	v_pk_fma_f32 v[144:145], v[110:111], v[10:11], v[144:145]
	v_pk_fma_f32 v[142:143], v[102:103], v[2:3], v[142:143]
	v_pk_fma_f32 v[140:141], v[106:107], v[14:15], v[140:141]
	v_pk_fma_f32 v[138:139], v[98:99], v[6:7], v[138:139]
	v_pk_add_f32 v[130:131], v[132:133], v[130:131]
	v_pk_add_f32 v[138:139], v[138:139], v[140:141]
	v_pk_add_f32 v[140:141], v[142:143], v[144:145]
	v_pk_add_f32 v[142:143], v[146:147], v[148:149]
	v_pk_add_f32 v[144:145], v[154:155], v[156:157]
	v_pk_add_f32 v[132:133], v[130:131], v[130:131] op_sel:[0,1] op_sel_hi:[1,0]
	v_pk_add_f32 v[142:143], v[144:145], v[142:143]
	v_pk_add_f32 v[138:139], v[140:141], v[138:139]
	v_add_f32_e32 v133, v142, v143
	v_add_f32_e32 v130, v138, v139
	s_waitcnt lgkmcnt(2)
	v_pk_mul_f32 v[138:139], v[90:91], v[54:55]
	s_waitcnt lgkmcnt(0)
	v_pk_mul_f32 v[140:141], v[94:95], v[62:63]
	v_pk_mul_f32 v[142:143], v[82:83], v[50:51]
	v_pk_mul_f32 v[144:145], v[86:87], v[58:59]
	v_pk_mul_f32 v[146:147], v[92:93], v[56:57]
	v_pk_mul_f32 v[148:149], v[96:97], v[64:65]
	v_pk_mul_f32 v[154:155], v[84:85], v[52:53]
	v_pk_mul_f32 v[156:157], v[88:89], v[60:61]
	v_add_f32_e32 v130, v130, v133
	v_pk_fma_f32 v[156:157], v[80:81], v[12:13], v[156:157]
	v_pk_fma_f32 v[154:155], v[72:73], v[4:5], v[154:155]
	v_pk_fma_f32 v[148:149], v[76:77], v[16:17], v[148:149]
	v_pk_fma_f32 v[146:147], v[68:69], v[8:9], v[146:147]
	v_pk_fma_f32 v[144:145], v[78:79], v[10:11], v[144:145]
	v_pk_fma_f32 v[142:143], v[70:71], v[2:3], v[142:143]
	v_pk_fma_f32 v[140:141], v[74:75], v[14:15], v[140:141]
	v_pk_fma_f32 v[138:139], v[66:67], v[6:7], v[138:139]
	v_mov_b32_e32 v133, v130
	v_pk_add_f32 v[138:139], v[138:139], v[140:141]
	v_pk_add_f32 v[140:141], v[142:143], v[144:145]
	v_pk_add_f32 v[142:143], v[146:147], v[148:149]
	v_pk_add_f32 v[144:145], v[154:155], v[156:157]
	v_permlane32_swap_b32_e32 v130, v133
	v_pk_add_f32 v[142:143], v[144:145], v[142:143]
	v_add_f32_e32 v160, v130, v133
	v_pk_add_f32 v[138:139], v[140:141], v[138:139]
	v_add_f32_e32 v133, v142, v143
	v_pk_add_f32 v[140:141], v[26:27], v[42:43]
	v_pk_add_f32 v[142:143], v[28:29], v[44:45]
	v_pk_add_f32 v[144:145], v[20:21], v[36:37]
	v_pk_add_f32 v[146:147], v[32:33], v[48:49]
	v_pk_add_f32 v[148:149], v[24:25], v[40:41]
	v_pk_add_f32 v[154:155], v[30:31], v[46:47]
	v_pk_add_f32 v[156:157], v[22:23], v[38:39]
	v_pk_add_f32 v[158:159], v[18:19], v[34:35]
	v_pk_add_f32 v[154:155], v[156:157], v[154:155]
	v_pk_add_f32 v[146:147], v[148:149], v[146:147]
	v_pk_add_f32 v[142:143], v[144:145], v[142:143]
	v_pk_add_f32 v[140:141], v[158:159], v[140:141]
	v_pk_add_f32 v[142:143], v[142:143], v[146:147]
	v_pk_add_f32 v[140:141], v[140:141], v[154:155]
	v_add_f32_e32 v130, v138, v139
	v_add_f32_e32 v140, v141, v140
	v_add_f32_e32 v141, v142, v143
	v_add_f32_e32 v133, v130, v133
	v_add_f32_e32 v140, v140, v141
	v_mov_b32_e32 v131, v132
	v_mov_b32_e32 v130, v140
	s_nop 1
	v_permlane32_swap_b32_e32 v140, v130
	v_add_f32_e32 v130, v140, v130
	v_fmamk_f32 v49, v130, 0xbc800000, v49
	v_fmamk_f32 v48, v130, 0xbc800000, v48
	v_fmamk_f32 v47, v130, 0xbc800000, v47
	v_fmamk_f32 v46, v130, 0xbc800000, v46
	v_fmamk_f32 v45, v130, 0xbc800000, v45
	v_fmamk_f32 v44, v130, 0xbc800000, v44
	v_fmamk_f32 v43, v130, 0xbc800000, v43
	v_fmamk_f32 v42, v130, 0xbc800000, v42
	v_fmamk_f32 v41, v130, 0xbc800000, v41
	v_fmamk_f32 v40, v130, 0xbc800000, v40
	v_fmamk_f32 v39, v130, 0xbc800000, v39
	v_fmamk_f32 v38, v130, 0xbc800000, v38
	v_fmamk_f32 v37, v130, 0xbc800000, v37
	v_fmamk_f32 v36, v130, 0xbc800000, v36
	v_fmamk_f32 v35, v130, 0xbc800000, v35
	v_fmac_f32_e32 v34, 0xbc800000, v130
	v_fmamk_f32 v33, v130, 0xbc800000, v33
	v_fmamk_f32 v32, v130, 0xbc800000, v32
	v_fmamk_f32 v31, v130, 0xbc800000, v31
	v_fmamk_f32 v30, v130, 0xbc800000, v30
	v_fmamk_f32 v29, v130, 0xbc800000, v29
	v_fmamk_f32 v28, v130, 0xbc800000, v28
	v_fmamk_f32 v27, v130, 0xbc800000, v27
	v_fmamk_f32 v26, v130, 0xbc800000, v26
	v_fmamk_f32 v25, v130, 0xbc800000, v25
	v_fmamk_f32 v24, v130, 0xbc800000, v24
	v_fmamk_f32 v23, v130, 0xbc800000, v23
	v_fmamk_f32 v22, v130, 0xbc800000, v22
	v_fmamk_f32 v21, v130, 0xbc800000, v21
	v_fmamk_f32 v20, v130, 0xbc800000, v20
	v_fmamk_f32 v19, v130, 0xbc800000, v19
	v_fmac_f32_e32 v18, 0xbc800000, v130
	v_pk_mul_f32 v[140:141], v[38:39], v[38:39]
	v_pk_mul_f32 v[142:143], v[46:47], v[46:47]
	v_pk_mul_f32 v[144:145], v[34:35], v[34:35]
	v_pk_mul_f32 v[146:147], v[42:43], v[42:43]
	v_pk_mul_f32 v[148:149], v[40:41], v[40:41]
	v_pk_mul_f32 v[154:155], v[48:49], v[48:49]
	v_pk_mul_f32 v[156:157], v[36:37], v[36:37]
	v_pk_mul_f32 v[158:159], v[44:45], v[44:45]
	v_pk_fma_f32 v[156:157], v[20:21], v[20:21], v[156:157]
	v_pk_fma_f32 v[158:159], v[28:29], v[28:29], v[158:159]
	v_pk_fma_f32 v[154:155], v[32:33], v[32:33], v[154:155]
	v_pk_fma_f32 v[148:149], v[24:25], v[24:25], v[148:149]
	v_pk_fma_f32 v[146:147], v[26:27], v[26:27], v[146:147]
	v_pk_fma_f32 v[144:145], v[18:19], v[18:19], v[144:145]
	v_pk_fma_f32 v[142:143], v[30:31], v[30:31], v[142:143]
	v_pk_fma_f32 v[140:141], v[22:23], v[22:23], v[140:141]
	v_permlane32_swap_b32_e32 v132, v131
	v_pk_add_f32 v[140:141], v[140:141], v[142:143]
	v_pk_add_f32 v[142:143], v[144:145], v[146:147]
	v_pk_add_f32 v[144:145], v[148:149], v[154:155]
	v_pk_add_f32 v[146:147], v[156:157], v[158:159]
	v_pk_add_f32 v[140:141], v[142:143], v[140:141]
	v_pk_add_f32 v[144:145], v[146:147], v[144:145]
	v_pk_mul_f32 v[122:123], v[122:123], v[38:39]
	v_pk_mov_b32 v[142:143], v[140:141], v[144:145] op_sel:[1,0]
	v_mov_b32_e32 v141, v145
	v_pk_add_f32 v[140:141], v[142:143], v[140:141]
	v_pk_mul_f32 v[126:127], v[126:127], v[46:47]
	v_pk_add_f32 v[140:141], v[140:141], v[140:141] op_sel:[0,1] op_sel_hi:[1,0]
	v_pk_mul_f32 v[114:115], v[114:115], v[34:35]
	v_mov_b32_e32 v130, v140
	s_nop 1
	v_permlane32_swap_b32_e32 v140, v130
	v_mov_b32_e32 v141, v132
	v_pk_add_f32 v[130:131], v[140:141], v[130:131]
	v_pk_mul_f32 v[118:119], v[118:119], v[42:43]
	v_pk_fma_f32 v[130:131], v[130:131], s[0:1], v[152:153] op_sel_hi:[1,0,0]
	v_pk_mul_f32 v[124:125], v[124:125], v[40:41]
	v_pk_mul_f32 v[128:129], v[128:129], v[48:49]
	v_pk_mul_f32 v[116:117], v[116:117], v[36:37]
	v_pk_mul_f32 v[120:121], v[120:121], v[44:45]
	v_pk_fma_f32 v[112:113], v[112:113], v[28:29], v[120:121]
	v_pk_fma_f32 v[104:105], v[104:105], v[20:21], v[116:117]
	v_pk_fma_f32 v[108:109], v[108:109], v[32:33], v[128:129]
	v_pk_fma_f32 v[100:101], v[100:101], v[24:25], v[124:125]
	v_pk_fma_f32 v[110:111], v[110:111], v[26:27], v[118:119]
	v_pk_fma_f32 v[102:103], v[102:103], v[18:19], v[114:115]
	v_pk_fma_f32 v[106:107], v[106:107], v[30:31], v[126:127]
	v_pk_fma_f32 v[98:99], v[98:99], v[22:23], v[122:123]
	v_rsq_f32_e32 v131, v131
	v_pk_add_f32 v[98:99], v[98:99], v[106:107]
	v_pk_add_f32 v[102:103], v[102:103], v[110:111]
	v_pk_add_f32 v[100:101], v[100:101], v[108:109]
	v_pk_add_f32 v[104:105], v[104:105], v[112:113]
	v_rsq_f32_e32 v132, v130
	v_pk_add_f32 v[100:101], v[104:105], v[100:101]
	v_pk_add_f32 v[98:99], v[102:103], v[98:99]
	v_add_f32_e32 v98, v98, v99
	v_add_f32_e32 v99, v100, v101
	v_add_f32_e32 v98, v98, v99
	v_mov_b32_e32 v99, v98
	v_pk_mul_f32 v[90:91], v[90:91], v[38:39]
	v_pk_mul_f32 v[94:95], v[94:95], v[46:47]
	v_pk_mul_f32 v[82:83], v[82:83], v[34:35]
	v_pk_mul_f32 v[86:87], v[86:87], v[42:43]
	v_permlane32_swap_b32_e32 v98, v99
	v_pk_fma_f32 v[78:79], v[78:79], v[26:27], v[86:87]
	v_pk_fma_f32 v[70:71], v[70:71], v[18:19], v[82:83]
	v_pk_fma_f32 v[74:75], v[74:75], v[30:31], v[94:95]
	v_pk_fma_f32 v[66:67], v[66:67], v[22:23], v[90:91]
	v_mov_b32_e32 v130, v131
	v_mov_b32_e32 v131, v132
	v_add_f32_e32 v98, v98, v99
	v_pk_add_f32 v[66:67], v[66:67], v[74:75]
	v_pk_add_f32 v[70:71], v[70:71], v[78:79]
	v_mul_f32_e32 v139, v160, v130
	v_mul_f32_e32 v98, v98, v131
	v_pk_add_f32 v[66:67], v[70:71], v[66:67]
	v_cmp_gt_u32_e32 vcc, 32, v1
	v_add_f32_e32 v66, v66, v67
	v_pk_mul_f32 v[92:93], v[92:93], v[40:41]
	v_cndmask_b32_e32 v67, v98, v139, vcc
	v_add_f32_e32 v67, s12, v67
	v_pk_mul_f32 v[96:97], v[96:97], v[48:49]
	v_pk_mul_f32 v[84:85], v[84:85], v[36:37]
	v_pk_mul_f32 v[88:89], v[88:89], v[44:45]
	v_mul_f32_e32 v67, 0xbfb8aa3b, v67
	v_pk_fma_f32 v[80:81], v[80:81], v[28:29], v[88:89]
	v_pk_fma_f32 v[72:73], v[72:73], v[20:21], v[84:85]
	v_pk_fma_f32 v[76:77], v[76:77], v[32:33], v[96:97]
	v_pk_fma_f32 v[68:69], v[68:69], v[24:25], v[92:93]
	v_exp_f32_e32 v70, v67
	v_pk_add_f32 v[68:69], v[68:69], v[76:77]
	v_pk_add_f32 v[72:73], v[72:73], v[80:81]
	v_cmp_lt_i32_e64 s[0:1], 0, v151
	v_pk_add_f32 v[68:69], v[72:73], v[68:69]
	v_mov_b32_e32 v137, v136
	v_add_f32_e32 v67, v68, v69
	v_add_f32_e32 v67, v66, v67
	v_add_f32_e32 v66, 1.0, v70
	v_rcp_f32_e32 v66, v66
	v_mov_b32_e32 v69, 0xff800000
	v_mov_b32_e32 v138, v133
	v_mov_b32_e32 v68, v67
	v_cndmask_b32_e64 v70, v69, v66, s[0:1]
	v_mbcnt_lo_u32_b32 v66, -1, 0
	v_mbcnt_hi_u32_b32 v66, -1, v66
	v_permlane32_swap_b32_e32 v136, v137
	v_permlane32_swap_b32_e32 v133, v138
	v_permlane32_swap_b32_e32 v67, v68
	v_and_b32_e32 v86, 64, v66
	s_mov_b32 s14, 8
	s_mov_b32 s13, 0
	v_mov_b32_e32 v66, 0
	s_waitcnt lgkmcnt(0)
